# P7: workgroup 0's tile->expert table built by an expert-parallel fill loop (each of 32 lanes writes its own tile range) instead of 32 broadcast shuffles x 5 compare/add chains; removes the phase's sin
# speedup vs baseline: 1.0004x; 1.0004x over previous
.LBB0_724:
	s_or_b64 exec, exec, s[4:5]
	v_add_u32_e32 v6, -1, v4
	v_cmp_lt_i32_e32 vcc, v6, v1
	v_add_u32_e32 v16, 0xff, v5
	v_and_b32_e32 v16, 0xffffff00, v16
	v_cndmask_b32_e32 v6, v6, v4, vcc
	v_lshlrev_b32_e32 v6, 2, v6
	ds_bpermute_b32 v6, v6, v16
	v_add_u32_e32 v7, -2, v4
	v_cmp_lt_i32_e32 vcc, v7, v1
	v_add_u32_e32 v17, -4, v4
	v_cmp_lt_i32_e64 s[4:5], v17, v1
	v_cndmask_b32_e32 v7, v7, v4, vcc
	v_cmp_eq_u32_e32 vcc, 0, v237
	v_lshlrev_b32_e32 v7, 2, v7
	v_cndmask_b32_e64 v17, v17, v4, s[4:5]
	s_waitcnt lgkmcnt(0)
	v_cndmask_b32_e64 v6, v6, 0, vcc
	v_add_u32_e32 v6, v6, v16
	ds_bpermute_b32 v7, v7, v6
	v_cmp_lt_u32_e64 s[4:5], 1, v237
	v_lshlrev_b32_e32 v17, 2, v17
	v_add_u32_e32 v18, -8, v4
	s_waitcnt lgkmcnt(0)
	v_cndmask_b32_e64 v7, 0, v7, s[4:5]
	v_add_u32_e32 v6, v7, v6
	ds_bpermute_b32 v7, v17, v6
	v_cmp_lt_i32_e64 s[4:5], v18, v1
	s_nop 1
	v_cndmask_b32_e64 v17, v18, v4, s[4:5]
	v_cmp_lt_u32_e64 s[4:5], 3, v237
	v_lshlrev_b32_e32 v17, 2, v17
	v_add_u32_e32 v18, -16, v4
	s_waitcnt lgkmcnt(0)
	v_cndmask_b32_e64 v7, 0, v7, s[4:5]
	v_add_u32_e32 v6, v7, v6
	ds_bpermute_b32 v7, v17, v6
	v_cmp_lt_i32_e64 s[4:5], v18, v1
	s_nop 1
	v_cndmask_b32_e64 v17, v18, v4, s[4:5]
	v_cmp_lt_u32_e64 s[4:5], 7, v237
	v_lshlrev_b32_e32 v17, 2, v17
	v_subrev_u32_e32 v18, 32, v4
	s_waitcnt lgkmcnt(0)
	v_cndmask_b32_e64 v7, 0, v7, s[4:5]
	v_add_u32_e32 v6, v7, v6
	ds_bpermute_b32 v7, v17, v6
	v_cmp_lt_i32_e64 s[4:5], v18, v1
	s_nop 1
	v_cndmask_b32_e64 v17, v18, v4, s[4:5]
	v_cmp_lt_u32_e64 s[4:5], 15, v237
	v_lshlrev_b32_e32 v17, 2, v17
	s_waitcnt lgkmcnt(0)
	v_cndmask_b32_e64 v7, 0, v7, s[4:5]
	v_add_u32_e32 v6, v7, v6
	ds_bpermute_b32 v7, v17, v6
	s_or_b32 s4, s80, s30
	s_cmp_lg_u32 s4, 0
	s_waitcnt lgkmcnt(0)
	v_cndmask_b32_e64 v7, v7, 0, s[0:1]
	v_add_u32_e32 v17, v7, v6
	s_cbranch_scc1 .LBB0_730
	v_lshlrev_b32_e32 v6, 2, v4
	v_and_b32_e32 v50, 0x100, v6
	v_or_b32_e32 v6, 0x7c, v50
	s_mov_b64 s[10:11], exec
	v_sub_u32_e32 v18, v17, v16
	v_ashrrev_i32_e32 v18, 8, v18
	v_ashrrev_i32_e32 v19, 8, v17
	v_mov_b32_e32 v20, 0x120
	v_cmp_eq_u32_e32 vcc, 31, v237
	s_nop 1
	v_cndmask_b32_e32 v19, v19, v20, vcc
	v_min_i32_e32 v19, v19, v20
	v_lshlrev_b32_e32 v21, 2, v18
	v_cmp_gt_u32_e32 vcc, 32, v237
	s_and_b64 exec, exec, vcc
.Lp7_tile_loop:
	v_cmp_lt_i32_e32 vcc, v18, v19
	s_and_b64 exec, exec, vcc
	s_cbranch_execz .Lp7_tile_done
	global_store_dword v21, v237, s[6:7]
	v_add_u32_e32 v18, 1, v18
	v_add_u32_e32 v21, 4, v21
	s_branch .Lp7_tile_loop
.Lp7_tile_done:
.LBB0_727:
	s_or_b64 exec, exec, s[10:11]
	v_cmp_eq_u32_e32 vcc, 0, v237
	ds_bpermute_b32 v6, v6, v17
	s_and_saveexec_b64 s[0:1], vcc
	s_cbranch_execz .LBB0_729
	s_waitcnt lgkmcnt(0)
	v_ashrrev_i32_e32 v6, 8, v6
	v_mov_b32_e32 v7, 0x780000
	global_store_dword v7, v6, s[88:89] offset:1200
